# hoisted four-waves-per-row version with the scanner waves at priority 2, so the gatherer wave sharing the SIMD cannot delay the scanner's refills
# speedup vs baseline: 1.0025x; 1.0025x over previous
.LBB1_217:
	s_andn2_saveexec_b64 s[0:1], s[30:31]
	s_cbranch_execz .LBB1_384
	s_setprio 2
	v_readfirstlane_b32 s34, v1
	v_readfirstlane_b32 s36, v84
	v_and_b32_e32 v3, 63, v0
	v_lshlrev_b32_e32 v2, 4, v3
	s_cmp_lt_i32 s36, 0
	s_cbranch_scc1 .LBB1_384
	s_add_i32 s36, s36, 1
	s_lshl_b32 s36, s36, 2
	s_sub_i32 s36, s36, 1
	s_lshr_b32 s33, s33, 2
	s_mov_b32 s55, s34
	s_mul_i32 s43, s55, 0x2800
	s_and_b32 s56, s2, 7
	s_lshr_b32 s57, s2, 3
	s_mul_i32 s37, s56, 31
	s_min_u32 s56, s56, 2
	s_add_u32 s37, s37, s56
	s_add_u32 s37, s37, s57
	s_waitcnt lgkmcnt(0)
	s_and_b32 s29, s29, 0xffff
	s_mov_b32 s30, 0x17d78400
	s_mov_b32 s31, 0x20000
	s_mov_b32 s35, 0
	s_movk_i32 s7, 0x40
	s_mov_b32 s9, 0x7fffffff
	s_lshl_b32 s44, s34, 12
	s_add_u32 s44, s44, 0x4000
	s_lshl_b32 s45, s34, 10
	s_add_u32 s45, s45, 0x8000
	s_lshl_b32 s46, s34, 4
	s_add_u32 s46, s46, 0x9000
	s_and_b32 s47, s37, 1
	s_lshl_b32 s47, s47, 2
	s_mul_i32 s38, s37, 0x9c40
	s_lshl_b32 s40, s47, 4
	s_sub_u32 s38, s38, s40
	s_add_u32 s38, s38, s43
	v_subrev_u32_e32 v8, s47, v3
	v_lshlrev_b32_e32 v8, 2, v8
	s_mul_i32 s40, s55, 0xa00
	v_add_u32_e32 v8, s40, v8
	s_mov_b64 s[48:49], -1
	s_mov_b64 s[50:51], -1
	v_mov_b32_e32 v5, v2
	v_mov_b32_e32 v6, v2
	v_mov_b32_e32 v7, v2
	s_cmp_lg_u32 s55, 0
	s_cbranch_scc1 .Lsc_i0
	s_lshl_b64 s[48:49], -1, s47
	v_max_u32_e32 v5, s47, v3
	v_lshlrev_b32_e32 v5, 4, v5
